# HGRN filler store step: precomputed per-lane destination offset + slot-linear scalar base, LDS reads hoisted to the top of the step (on top of HGRN load + attention filler address strength reduction +
# speedup vs baseline: 1.0190x; 1.0036x over previous
; DEV int ltid() { int t = threadIdx.x; asm volatile("" : "+v"(t)); return t; }
; DEV void fill_store(CParams& p, int wg, int slot, int bufsel) {
;   extern __shared__ __attribute__((aligned(16))) char shm[];
;   const unsigned* T = (const unsigned*)(shm + FILL_LDS_OFF + bufsel * FILL_TB); const int tid = ltid(), nl = tid >> 3, cc = tid & 7;
;   const FillDesc d = fill_decode(p, wg, slot);
;   u32x4 v; v.x = T[nl * 33 + 4 * cc]; v.y = T[nl * 33 + 4 * cc + 1]; v.z = T[nl * 33 + 4 * cc + 2]; v.w = T[nl * 33 + 4 * cc + 3];
;   *(u32x4*)(d.dst + (long)perm_row(d.perm, d.n0 + nl) * 2048 + d.kh + 16 * cc) = v;
; DEV void hgrn_unit(CParams& p, int u, int wg, bool fill) {
;     ...
;   const int sl = u & 3, dir = (u >> 2) & 1, h = (u >> 3) & 7, b = u >> 6;
;   const int tid = ltid(), wid = tid >> 6, lane = tid & 63, fr = lane & 15, fq = lane >> 4;
;   const int dp = lane & 7, seg = lane >> 3, d0 = 16 * wid + 2 * dp;
;   const float* G = dir ? p.gb : p.gf;
;   bf16_t* O = dir ? p.ob : p.of;
;   const int sgn = dir ? -1 : 1;
;     ...
;   f32x4 S[2] = {{0.f, 0.f, 0.f, 0.f}, {0.f, 0.f, 0.f, 0.f}};
;   float dec = 0.f;
;   f32x2 g[8]; unsigned q[8]; u32x2 v;
;   f32x2 gN[8]; unsigned qN[8]; u32x2 vN;
.LBB0_766:
	v_or_b32_e32 v18, v108, v109
	v_mov_b32_e32 v22, v0
	v_add_u32_e32 v194, v18, v116
	v_add_u32_e32 v195, v18, v110
	s_lshl_b32 s21, s24, s21
	s_lshl_b32 s22, s24, 7
	v_ashrrev_i32_e32 v18, 2, v22
	s_and_b32 s21, s21, 0x780
	v_and_b32_e32 v18, -4, v18
	s_and_b32 s22, s22, 0x780
	v_add_u32_e32 v18, s21, v18
	s_or_b32 s25, s22, s3
	v_mad_i64_i32 v[18:19], s[22:23], s20, v18, 0
	v_lshl_add_u64 v[18:19], v[18:19], 2, s[18:19]
	s_lshl_b32 s62, s25, 2
	s_mov_b32 s63, 0
	v_lshl_add_u64 v[20:21], v[18:19], 0, s[62:63]
	v_lshlrev_b32_e32 v18, 4, v22
	v_and_b32_e32 v18, 0xf0, v18
	v_mov_b32_e32 v19, 0
	v_lshl_add_u64 v[20:21], v[20:21], 0, v[18:19]
	s_lshl_b32 s62, s20, 2
	v_lshl_add_u64 v[30:31], v[20:21], 0, s[62:63]
	global_load_dwordx4 v[22:25], v[20:21], off
	global_load_dwordx4 v[26:29], v[30:31], off
	v_lshl_add_u64 v[20:21], v[30:31], 0, s[62:63]
	s_waitcnt lgkmcnt(12)
	v_cndmask_b32_e64 v130, v36, v35, s[12:13]
	v_lshl_add_u64 v[48:49], v[20:21], 0, s[62:63]
	global_load_dwordx4 v[30:33], v[20:21], off
	global_load_dwordx4 v[34:37], v[48:49], off
	s_add_u32 s16, s16, s56
	s_addc_u32 s17, s17, 0
	s_add_u32 s16, s16, s60
	s_addc_u32 s17, s17, 0
	v_mov_b32_e32 v59, v19
	v_lshl_add_u64 v[108:109], s[16:17], 0, v[58:59]
	s_add_u32 s16, s58, s56
	s_addc_u32 s17, s59, 0
	v_ashrrev_i32_e32 v48, 7, v112
	s_add_u32 s16, s16, s60
	v_lshl_or_b32 v18, v48, 4, v113
	s_movk_i32 s62, 0x110
	v_and_b32_e32 v106, 16, v106
	s_addc_u32 s17, s17, 0
	v_mul_lo_u32 v49, v18, s62
	v_lshlrev_b32_e32 v52, 1, v18
	v_mul_lo_u32 v103, v18, s36
	v_lshlrev_b32_e32 v18, 1, v106
	v_or_b32_e32 v47, 3, v102
	v_lshl_add_u64 v[20:21], s[16:17], 0, v[18:19]
	v_lshlrev_b32_e32 v18, 1, v102
	s_add_i32 s16, 0, 0x1e600
	s_add_i32 s61, 0, 0x10400
	s_waitcnt lgkmcnt(0)
	s_barrier
	s_load_dwordx4 s[44:47], s[14:15], 0xe8
	v_add_u32_e32 v202, 0, v49
	v_lshl_add_u64 v[110:111], v[20:21], 0, v[18:19]
	v_add3_u32 v204, s16, v51, v46
	s_load_dwordx2 s[64:65], s[14:15], 0xa0
	s_load_dwordx2 s[66:67], s[14:15], 0xb0
	v_add_u32_e32 v205, s61, v49
	v_or_b32_e32 v21, 64, v114
	v_or_b32_e32 v49, 0x80, v114
	v_or_b32_e32 v51, 0xc0, v114
	v_cmp_gt_u32_e64 s[24:25], v47, v113
	v_or_b32_e32 v47, 32, v46
	s_movk_i32 s26, 0x70
	v_bitop3_b32 v183, v46, v114, 16 bitop3:0x6c
	v_bitop3_b32 v182, v46, v21, 16 bitop3:0x6c
	v_bitop3_b32 v181, v46, v49, 16 bitop3:0x6c
	v_bitop3_b32 v180, v46, v51, 16 bitop3:0x6c
	v_bitop3_b32 v178, v47, v114, 48 bitop3:0x6c
	v_bitop3_b32 v177, v47, v21, 48 bitop3:0x6c
	v_bitop3_b32 v176, v47, v49, 48 bitop3:0x6c
	v_bitop3_b32 v175, v47, v51, 48 bitop3:0x6c
	v_or_b32_e32 v47, 64, v46
	s_movk_i32 s27, 0x50
	v_or_b32_e32 v46, 0x60, v46
	v_or_b32_e32 v53, v106, v113
	v_bitop3_b32 v207, v52, v21, s26 bitop3:0x6c
	v_bitop3_b32 v172, v47, v21, s27 bitop3:0x6c
	v_bitop3_b32 v165, v46, v21, s26 bitop3:0x6c
	v_mov_b32_e32 v21, s80
	v_mul_u32_u24_e32 v203, 0x110, v53
	v_mul_u32_u24_e32 v18, 0x48, v53
	v_add_u32_e32 v20, s16, v114
	s_movk_i32 s14, 0x80
	v_mad_u32_u24 v191, v113, s62, 0
	v_mad_u32_u24 v184, v113, s62, v21
	v_mul_u32_u24_e32 v192, 0x440, v70
	v_mul_u32_u24_e32 v193, 0x110, v50
	v_add_u32_e32 v196, 0x220, v194
	v_add_u32_e32 v197, 0x330, v194
	v_add_u32_e32 v198, 0x440, v194
	v_add_u32_e32 v199, 0x550, v194
	v_add_u32_e32 v200, 0x660, v194
	v_add_u32_e32 v201, 0x770, v194
	s_mov_b32 s57, 4
	v_mul_u32_u24_e32 v187, 0x90, v53
	v_lshl_add_u32 v188, v70, 3, 0
	v_add_u32_e32 v186, 0xfffffc00, v103
	v_bitop3_b32 v206, v52, v114, s26 bitop3:0x6c
	v_bitop3_b32 v208, v52, v49, s26 bitop3:0x6c
	v_bitop3_b32 v209, v52, v51, s26 bitop3:0x6c
	v_cmp_lt_i32_e64 s[16:17], -1, v48
	v_cmp_gt_u32_e64 s[38:39], s14, v112
	v_cmp_gt_u32_e64 s[18:19], v102, v113
	v_cmp_lt_u32_e64 s[20:21], v102, v113
	v_cmp_gt_u32_e64 s[22:23], v50, v113
	v_cmp_lt_i32_e64 s[36:37], 0, v48
	v_add_u32_e32 v190, 0x1100, v191
	v_cmp_eq_u32_e64 s[34:35], 1, v48
	v_cmp_lt_i32_e64 s[14:15], 1, v48
	v_add_u32_e32 v189, 0x2200, v191
	v_bitop3_b32 v173, v47, v114, s27 bitop3:0x6c
	v_bitop3_b32 v171, v47, v49, s27 bitop3:0x6c
	v_bitop3_b32 v170, v47, v51, s27 bitop3:0x6c
	v_cmp_eq_u32_e64 s[30:31], 2, v48
	v_cmp_lt_i32_e64 s[28:29], 2, v48
	v_bitop3_b32 v167, v46, v114, s26 bitop3:0x6c
	v_bitop3_b32 v164, v46, v49, s26 bitop3:0x6c
	v_bitop3_b32 v163, v46, v51, s26 bitop3:0x6c
	v_cmp_eq_u32_e64 s[26:27], 3, v48
	v_add_u32_e32 v179, 0x1100, v184
	v_add_u32_e32 v174, 0x2200, v184
	v_add_u32_e32 v166, 0x3300, v184
	v_add_lshl_u32 v210, v18, v102, 1
	s_add_i32 s82, s2, 0x700
	s_movk_i32 s83, 0x84
	s_movk_i32 s84, 0x7ff
	s_mov_b32 s85, 0xda24260
	v_mov_b32_e32 v211, 0xfffff800
	v_mov_b32_e32 v212, 0x80
	v_mov_b32_e32 v213, 0x7149f2ca
	v_add_u32_e32 v160, v20, v203
	s_mov_b32 s86, 0
	s_mov_b32 s87, 0
	v_readfirstlane_b32 s32, v82
	v_readfirstlane_b32 s92, v83
	v_readfirstlane_b32 s93, v84
	v_readfirstlane_b32 s94, v85
	v_readfirstlane_b32 s95, v108
	v_readfirstlane_b32 s96, v109
	s_nop 1
	v_subrev_u32_e32 v82, s32, v82
	v_add_u32_e32 v82, 0x40000, v82
	v_subrev_u32_e32 v108, s95, v108
	v_add_u32_e32 v108, 0x20000, v108
	v_lshl_add_u32 v151, v151, 12, v82
	v_lshl_add_u32 v135, v135, 12, v82
	v_lshl_add_u32 v136, v136, 12, v82
	v_lshl_add_u32 v137, v137, 12, v82
	v_lshl_add_u32 v138, v138, 12, v82
	v_lshl_add_u32 v139, v139, 12, v82
	v_lshl_add_u32 v141, v141, 12, v82
	v_lshl_add_u32 v143, v143, 12, v82
	v_lshl_add_u32 v144, v144, 11, v108
	s_waitcnt lgkmcnt(0)
	s_lshr_b32 s70, s2, 1
	s_and_b32 s71, s70, 31
	s_lshl_b32 s71, s71, 7
	s_or_b32 s71, s71, s3
	s_lshr_b32 s72, s70, 5
	s_lshl_b32 s72, s72, 7
	v_lshrrev_b32_e32 v20, 3, v0
	v_and_b32_e32 v21, 7, v0
	v_lshlrev_b32_e32 v21, 4, v21
	v_mul_u32_u24_e32 v212, 0x84, v20
	v_add_u32_e32 v212, v212, v21
	v_add_u32_e32 v211, s71, v20
	v_and_b32_e32 v46, 0x7ff, v211
	v_lshrrev_b32_e32 v211, 11, v211
	v_lshlrev_b32_e32 v211, 7, v211
	v_and_b32_e32 v47, 0x7f, v46
	v_or_b32_e32 v211, v211, v47
	v_lshrrev_b32_e32 v46, 7, v46
	v_lshl_or_b32 v211, v46, 8, v211
	v_lshlrev_b32_e32 v211, 11, v211
	v_add_u32_e32 v211, v211, v21
	v_add_u32_e32 v211, s72, v211
	s_branch .LBB0_770

; DEV int ltid() { int t = threadIdx.x; asm volatile("" : "+v"(t)); return t; }
; DEV void fill_store(CParams& p, int wg, int slot, int bufsel) {
;   extern __shared__ __attribute__((aligned(16))) char shm[];
;   const unsigned* T = (const unsigned*)(shm + FILL_LDS_OFF + bufsel * FILL_TB); const int tid = ltid(), nl = tid >> 3, cc = tid & 7;
;   const FillDesc d = fill_decode(p, wg, slot);
;   u32x4 v; v.x = T[nl * 33 + 4 * cc]; v.y = T[nl * 33 + 4 * cc + 1]; v.z = T[nl * 33 + 4 * cc + 2]; v.w = T[nl * 33 + 4 * cc + 3];
;   *(u32x4*)(d.dst + (long)perm_row(d.perm, d.n0 + nl) * 2048 + d.kh + 16 * cc) = v;
; }
.LBB0_770:
	s_add_i32 s88, s77, s87
	s_add_i32 s89, s77, s86
	s_add_i32 s62, s88, 0x137f
	s_add_i32 s70, s89, 0x480
	s_and_b64 s[68:69], s[52:53], exec
	s_cselect_b32 s62, s70, s62
	v_add_u32_e32 v21, s81, v212
	ds_read2_b32 v[46:47], v21 offset1:1
	ds_read2_b32 v[48:49], v21 offset0:2 offset1:3
	s_sub_u32 s70, s62, 64
	s_lshl_b32 s72, s70, 11
	s_lshl_b32 s70, s70, 12
	s_add_u32 s70, s32, s70
	s_addc_u32 s71, s92, 0
	s_add_u32 s72, s93, s72
	s_addc_u32 s73, s94, 0
	v_lshrrev_b32_e32 v20, 1, v151
	global_load_dword v250, v20, s[72:73]
	global_load_dwordx2 v[126:127], v151, s[70:71]
	v_lshrrev_b32_e32 v21, 1, v135
	global_load_dword v249, v21, s[72:73]
	global_load_dwordx2 v[124:125], v135, s[70:71]
	v_lshrrev_b32_e32 v20, 1, v136
	global_load_dword v248, v20, s[72:73]
	global_load_dwordx2 v[122:123], v136, s[70:71]
	v_lshrrev_b32_e32 v21, 1, v137
	global_load_dword v247, v21, s[72:73]
	global_load_dwordx2 v[120:121], v137, s[70:71]
	v_lshrrev_b32_e32 v20, 1, v138
	global_load_dword v242, v20, s[72:73]
	global_load_dwordx2 v[118:119], v138, s[70:71]
	v_lshrrev_b32_e32 v21, 1, v139
	global_load_dword v240, v21, s[72:73]
	global_load_dwordx2 v[116:117], v139, s[70:71]
	v_lshrrev_b32_e32 v20, 1, v141
	global_load_dword v239, v20, s[72:73]
	global_load_dwordx2 v[114:115], v141, s[70:71]
	v_lshrrev_b32_e32 v21, 1, v143
	global_load_dword v238, v21, s[72:73]
	global_load_dwordx2 v[112:113], v143, s[70:71]
	s_sub_u32 s70, s62, 64
	s_lshl_b32 s70, s70, 11
	s_add_u32 s70, s95, s70
	s_addc_u32 s71, s96, 0
	global_load_dwordx2 v[128:129], v144, s[70:71]
	s_add_i32 s91, s82, 0xfffffc00
	s_lshr_b32 s70, s91, 8
	s_lshr_b32 s71, s70, 2
	s_lshl_b32 s71, s71, 23
	s_and_b32 s70, s70, 3
	s_lshl_b32 s70, s70, 9
	s_or_b32 s70, s70, s71
	s_add_u32 s72, s44, s70
	s_addc_u32 s73, s45, 0
	s_waitcnt lgkmcnt(0)
	global_store_dwordx4 v211, v[46:49], s[72:73]
	v_add_u32_e32 v215, v202, v206
	v_add_u32_e32 v219, v202, v208
	v_add_u32_e32 v216, v202, v207
	ds_read_b128 v[58:61], v215
	ds_read_b128 v[50:53], v216
	v_add_u32_e32 v220, v202, v209
	ds_read_b128 v[54:57], v219
	ds_read_b128 v[46:49], v220
	v_mov_b32_e32 v62, 0
	v_mov_b32_e32 v66, 0
	v_mov_b32_e32 v67, 0
	v_mov_b32_e32 v68, 0
	v_mov_b32_e32 v69, 0
	s_and_saveexec_b64 s[68:69], s[16:17]
	s_cbranch_execz .LBB0_780
	v_add_u32_e32 v18, v191, v183
	ds_read_b128 v[64:67], v18 offset:17408
	v_add_u32_e32 v18, v191, v182
	ds_read_b128 v[68:71], v18 offset:17408
	v_add_u32_e32 v18, v191, v181
	ds_read_b128 v[72:75], v18 offset:17408
	v_add_u32_e32 v18, v191, v180
	s_waitcnt lgkmcnt(2)
	v_mfma_f32_16x16x32_bf16 v[64:67], v[64:67], v[58:61], 0
	s_waitcnt lgkmcnt(1)
	v_mfma_f32_16x16x32_bf16 v[64:67], v[68:71], v[50:53], v[64:67]
	ds_read_b128 v[68:71], v18 offset:17408
	s_waitcnt lgkmcnt(1)
	v_mfma_f32_16x16x32_bf16 v[64:67], v[72:75], v[54:57], v[64:67]
	s_waitcnt lgkmcnt(0)
	v_mfma_f32_16x16x32_bf16 v[66:69], v[68:71], v[46:49], v[64:67]
	s_and_saveexec_b64 s[70:71], s[38:39]
	s_nop 6
	v_cndmask_b32_e64 v66, v66, 0, s[18:19]
	v_cndmask_b32_e64 v67, 0, v67, s[20:21]
	v_cndmask_b32_e64 v68, v68, 0, s[22:23]
	v_cndmask_b32_e64 v69, v69, 0, s[24:25]
	s_or_b64 exec, exec, s[70:71]

; DEV int ltid() { int t = threadIdx.x; asm volatile("" : "+v"(t)); return t; }
; DEV unsigned cvt_pk4_fp8(f32x4 v) { unsigned r = 0; r = __builtin_amdgcn_cvt_pk_fp8_f32(v[0], v[1], r, false); r = __builtin_amdgcn_cvt_pk_fp8_f32(v[2], v[3], r, true); return r; }
; DEV void fill_load(CParams& p, int wg, int slot, f32x4 (&ld)[4]) {
;   const FillDesc d = fill_decode(p, wg, slot); const int tid = ltid(), tx = tid & 15, ty = tid >> 4;
;   const float* sp = d.src + (long)(d.kh + 4 * ty) * d.ldsrc + d.n0 + 4 * tx;
; #pragma unroll
;   for (int r = 0; r < 4; ++r) ld[r] = *(const f32x4*)(sp + (long)r * d.ldsrc);
; }
; DEV void fill_write(const f32x4 (&ld)[4], int bufsel) {
;   extern __shared__ __attribute__((aligned(16))) char shm[];
;   unsigned* T = (unsigned*)(shm + FILL_LDS_OFF + bufsel * FILL_TB); const int tid = ltid(), tx = tid & 15, ty = tid >> 4;
;   constexpr float WS = (float)(1 << FP8_WSCALE_LOG2_);
; #pragma unroll
;   for (int j = 0; j < 4; ++j) T[(4 * tx + j) * 33 + ty] = cvt_pk4_fp8((f32x4){ld[0][j] * WS, ld[1][j] * WS, ld[2][j] * WS, ld[3][j] * WS});
; }
; DEV void fill_store(CParams& p, int wg, int slot, int bufsel) {
;   extern __shared__ __attribute__((aligned(16))) char shm[];
;   const unsigned* T = (const unsigned*)(shm + FILL_LDS_OFF + bufsel * FILL_TB); const int tid = ltid(), nl = tid >> 3, cc = tid & 7;
;   const FillDesc d = fill_decode(p, wg, slot);
;   u32x4 v; v.x = T[nl * 33 + 4 * cc]; v.y = T[nl * 33 + 4 * cc + 1]; v.z = T[nl * 33 + 4 * cc + 2]; v.w = T[nl * 33 + 4 * cc + 3];
;   *(u32x4*)(d.dst + (long)perm_row(d.perm, d.n0 + nl) * 2048 + d.kh + 16 * cc) = v;
; }
.LBB0_801:
	v_mov_b32_e32 v4, v0
	s_lshl_b32 s62, s72, s62
	s_lshl_b32 s71, s72, 7
	v_ashrrev_i32_e32 v2, 2, v4
	s_and_b32 s62, s62, 0x780
	v_and_b32_e32 v2, -4, v2
	s_and_b32 s71, s71, 0x780
	v_add_u32_e32 v2, s62, v2
	s_or_b32 s71, s71, s3
	v_mad_i64_i32 v[2:3], s[72:73], s70, v2, 0
	v_lshl_add_u64 v[2:3], v[2:3], 2, s[68:69]
	s_lshl_b32 s62, s71, 2
	v_lshlrev_b32_e32 v4, 4, v4
	v_lshl_add_u64 v[2:3], v[2:3], 0, s[62:63]
	v_and_b32_e32 v18, 0xf0, v4
	v_lshl_add_u64 v[2:3], v[2:3], 0, v[18:19]
	s_lshl_b32 s62, s70, 2
	v_lshl_add_u64 v[4:5], v[2:3], 0, s[62:63]
	global_load_dwordx4 v[10:13], v[2:3], off
	global_load_dwordx4 v[14:17], v[4:5], off
	v_lshl_add_u64 v[2:3], v[4:5], 0, s[62:63]
	v_lshl_add_u64 v[6:7], v[2:3], 0, s[62:63]
	s_add_i32 s62, s88, 0x133f
	s_add_i32 s70, s89, 0x4c0
	s_and_b64 s[68:69], s[52:53], exec
	s_cselect_b32 s62, s70, s62
	s_sub_u32 s70, s62, 64
	s_lshl_b32 s72, s70, 11
	s_lshl_b32 s70, s70, 12
	s_add_u32 s70, s32, s70
	s_addc_u32 s71, s92, 0
	s_add_u32 s72, s93, s72
	s_addc_u32 s73, s94, 0
	global_load_dwordx4 v[2:5], v[2:3], off
	s_nop 0
	global_load_dwordx4 v[6:9], v[6:7], off
	s_waitcnt lgkmcnt(0)
	s_barrier
	v_add_u32_e32 v21, s76, v212
	ds_read2_b32 v[46:47], v21 offset1:1
	ds_read2_b32 v[48:49], v21 offset0:2 offset1:3
	v_lshrrev_b32_e32 v20, 1, v151
	global_load_dword v169, v20, s[72:73]
	global_load_dwordx2 v[100:101], v151, s[70:71]
	v_lshrrev_b32_e32 v21, 1, v135
	global_load_dword v168, v21, s[72:73]
	global_load_dwordx2 v[98:99], v135, s[70:71]
	v_lshrrev_b32_e32 v20, 1, v136
	global_load_dword v162, v20, s[72:73]
	global_load_dwordx2 v[96:97], v136, s[70:71]
	v_lshrrev_b32_e32 v21, 1, v137
	global_load_dword v161, v21, s[72:73]
	global_load_dwordx2 v[94:95], v137, s[70:71]
	v_lshrrev_b32_e32 v20, 1, v138
	global_load_dword v159, v20, s[72:73]
	global_load_dwordx2 v[92:93], v138, s[70:71]
	v_lshrrev_b32_e32 v21, 1, v139
	global_load_dword v158, v21, s[72:73]
	global_load_dwordx2 v[90:91], v139, s[70:71]
	v_lshrrev_b32_e32 v20, 1, v141
	global_load_dword v157, v20, s[72:73]
	global_load_dwordx2 v[88:89], v141, s[70:71]
	v_lshrrev_b32_e32 v21, 1, v143
	global_load_dword v156, v21, s[72:73]
	global_load_dwordx2 v[86:87], v143, s[70:71]
	s_sub_u32 s70, s62, 64
	s_lshl_b32 s70, s70, 11
	s_add_u32 s70, s95, s70
	s_addc_u32 s71, s96, 0
	global_load_dwordx2 v[104:105], v144, s[70:71]
	s_add_i32 s91, s82, 0xfffffd00
	s_lshr_b32 s70, s91, 8
	s_lshr_b32 s71, s70, 2
	s_lshl_b32 s71, s71, 23
	s_and_b32 s70, s70, 3
	s_lshl_b32 s70, s70, 9
	s_or_b32 s70, s70, s71
	s_add_u32 s72, s44, s70
	s_addc_u32 s73, s45, 0
	s_waitcnt lgkmcnt(0)
	global_store_dwordx4 v211, v[46:49], s[72:73]
	v_add_u32_e32 v243, v205, v206
	v_add_u32_e32 v245, v205, v208
	v_add_u32_e32 v244, v205, v207
	ds_read_b128 v[58:61], v243
	ds_read_b128 v[50:53], v244
	v_add_u32_e32 v246, v205, v209
	ds_read_b128 v[54:57], v245
	ds_read_b128 v[46:49], v246
	v_mov_b32_e32 v62, 0
	v_mov_b32_e32 v66, 0
	v_mov_b32_e32 v67, 0
	v_mov_b32_e32 v68, 0
	v_mov_b32_e32 v69, 0
	s_and_saveexec_b64 s[68:69], s[16:17]
	s_cbranch_execz .LBB0_811
	v_add_u32_e32 v18, v184, v183
	ds_read_b128 v[64:67], v18
	v_add_u32_e32 v18, v184, v182
	ds_read_b128 v[68:71], v18
	v_add_u32_e32 v18, v184, v181
	ds_read_b128 v[72:75], v18
	v_add_u32_e32 v18, v184, v180
	s_waitcnt lgkmcnt(2)
	v_mfma_f32_16x16x32_bf16 v[64:67], v[64:67], v[58:61], 0
	s_waitcnt lgkmcnt(1)
	v_mfma_f32_16x16x32_bf16 v[64:67], v[68:71], v[50:53], v[64:67]
	ds_read_b128 v[68:71], v18
	s_waitcnt lgkmcnt(1)
	v_mfma_f32_16x16x32_bf16 v[64:67], v[72:75], v[54:57], v[64:67]
	s_waitcnt lgkmcnt(0)
	v_mfma_f32_16x16x32_bf16 v[66:69], v[68:71], v[46:49], v[64:67]
	s_and_saveexec_b64 s[70:71], s[38:39]
	s_nop 6
	v_cndmask_b32_e64 v66, v66, 0, s[18:19]
	v_cndmask_b32_e64 v67, 0, v67, s[20:21]
	v_cndmask_b32_e64 v68, v68, 0, s[22:23]
	v_cndmask_b32_e64 v69, v69, 0, s[24:25]
	s_or_b64 exec, exec, s[70:71]

; DEV FillDesc fill_decode(CParams& p, int wg, int slot) {
;   const int h = slot * 256 + wg, t = h >> 1, half = h & 1; FillDesc d;
;   if (t < NE * 512) { const int e = t >> 9, r = t & 511; d.src = p.w_gu + (long)e * 2048 * 4096; d.ldsrc = 4096; d.dst = p.wt_gu8 + (long)e * 4096 * 2048; d.perm = 2; d.n0 = (r & 31) * 128 + 64 * half; d.kh = (r >> 5) * 128; }
;   else { const int v = t - NE * 512, e = v >> 8, r = v & 255; d.src = p.w_dn + (long)e * 2048 * 2048; d.ldsrc = 2048; d.dst = p.wt_dn8 + (long)e * 2048 * 2048; d.perm = 0; d.n0 = (r & 15) * 128 + 64 * half; d.kh = (r >> 4) * 128; }
; DEV void hgrn_unit(CParams& p, int u, int wg, bool fill) {
;     ...
;   HG_STEP(66, true, true, fldA);
;   HG_MMA(67, true);
;   __syncthreads();
;   if (fill && FILL_HG == 67) fill_store(p, wg, 66, 0);
.LBB0_832:
	v_mov_b32_e32 v211, 0xfffff800
	v_mov_b32_e32 v212, 0x80
	s_add_i32 s68, s2, 0x4100
	s_ashr_i32 s57, s68, 1
	s_cmpk_lt_i32 s57, 0x4000
	v_mov_b32_e32 v18, v0
	s_cselect_b64 s[64:65], -1, 0
	s_cmpk_gt_i32 s57, 0x3fff
	s_cbranch_scc0 .LBB0_834
	s_add_i32 s61, s57, 0xffffc000
	s_lshr_b32 s62, s61, 8
	s_mov_b32 s63, 0
	s_lshl_b64 s[62:63], s[62:63], 22
	s_add_u32 s62, s46, s62
	s_addc_u32 s63, s47, s63
	s_mov_b32 s61, 3
	s_cbranch_execz .LBB0_835
	s_branch .LBB0_836

; DEV int ltid() { int t = threadIdx.x; asm volatile("" : "+v"(t)); return t; }
; DEV void fill_store(CParams& p, int wg, int slot, int bufsel) {
;   extern __shared__ __attribute__((aligned(16))) char shm[];
;   const unsigned* T = (const unsigned*)(shm + FILL_LDS_OFF + bufsel * FILL_TB); const int tid = ltid(), nl = tid >> 3, cc = tid & 7;
;   const FillDesc d = fill_decode(p, wg, slot);
;   u32x4 v; v.x = T[nl * 33 + 4 * cc]; v.y = T[nl * 33 + 4 * cc + 1]; v.z = T[nl * 33 + 4 * cc + 2]; v.w = T[nl * 33 + 4 * cc + 3];
;   *(u32x4*)(d.dst + (long)perm_row(d.perm, d.n0 + nl) * 2048 + d.kh + 16 * cc) = v;
; DEV void hgrn_unit(CParams& p, int u, int wg, bool fill) {
;     ...
;   const int sl = u & 3, dir = (u >> 2) & 1, h = (u >> 3) & 7, b = u >> 6;
;   const int tid = ltid(), wid = tid >> 6, lane = tid & 63, fr = lane & 15, fq = lane >> 4;
;   const int dp = lane & 7, seg = lane >> 3, d0 = 16 * wid + 2 * dp;
;   const float* G = dir ? p.gb : p.gf;
;   bf16_t* O = dir ? p.ob : p.of;
;   const int sgn = dir ? -1 : 1;
;     ...
;   f32x4 S[2] = {{0.f, 0.f, 0.f, 0.f}, {0.f, 0.f, 0.f, 0.f}};
;   float dec = 0.f;
;   f32x2 g[8]; unsigned q[8]; u32x2 v;
;   f32x2 gN[8]; unsigned qN[8]; u32x2 vN;
.LBB0_971:
	v_or_b32_e32 v18, v108, v109
	v_mov_b32_e32 v22, v0
	v_add_u32_e32 v195, v18, v116
	v_add_u32_e32 v196, v18, v111
	s_lshl_b32 s21, s25, s21
	s_lshl_b32 s22, s25, 7
	v_ashrrev_i32_e32 v18, 2, v22
	s_and_b32 s21, s21, 0x780
	v_and_b32_e32 v18, -4, v18
	s_and_b32 s22, s24, s22
	v_add_u32_e32 v18, s21, v18
	s_or_b32 s24, s22, s53
	v_mad_i64_i32 v[18:19], s[22:23], s20, v18, 0
	v_lshl_add_u64 v[18:19], v[18:19], 2, s[18:19]
	s_lshl_b32 s62, s24, 2
	s_mov_b32 s63, 0
	v_lshl_add_u64 v[20:21], v[18:19], 0, s[62:63]
	v_lshlrev_b32_e32 v18, 4, v22
	v_and_b32_e32 v18, 0xf0, v18
	v_mov_b32_e32 v19, 0
	v_lshl_add_u64 v[20:21], v[20:21], 0, v[18:19]
	s_lshl_b32 s62, s20, 2
	v_lshl_add_u64 v[30:31], v[20:21], 0, s[62:63]
	global_load_dwordx4 v[22:25], v[20:21], off
	global_load_dwordx4 v[26:29], v[30:31], off
	v_lshl_add_u64 v[20:21], v[30:31], 0, s[62:63]
	s_waitcnt lgkmcnt(12)
	v_cndmask_b32_e64 v130, v36, v35, s[12:13]
	v_lshl_add_u64 v[48:49], v[20:21], 0, s[62:63]
	global_load_dwordx4 v[30:33], v[20:21], off
	global_load_dwordx4 v[34:37], v[48:49], off
	s_add_u32 s16, s16, s56
	s_addc_u32 s17, s17, 0
	s_add_u32 s16, s16, s60
	s_addc_u32 s17, s17, 0
	v_mov_b32_e32 v59, v19
	v_lshl_add_u64 v[108:109], s[16:17], 0, v[58:59]
	s_add_u32 s16, s58, s56
	s_addc_u32 s17, s59, 0
	v_ashrrev_i32_e32 v48, 7, v112
	s_add_u32 s16, s16, s60
	v_lshl_or_b32 v18, v48, 4, v113
	s_movk_i32 s62, 0x110
	v_and_b32_e32 v106, 16, v110
	s_addc_u32 s17, s17, 0
	v_mul_lo_u32 v49, v18, s62
	v_lshlrev_b32_e32 v52, 1, v18
	v_mul_lo_u32 v107, v18, s36
	v_lshlrev_b32_e32 v18, 1, v106
	v_or_b32_e32 v47, 3, v254
	v_lshl_add_u64 v[20:21], s[16:17], 0, v[18:19]
	v_lshlrev_b32_e32 v18, 1, v254
	s_add_i32 s16, 0, 0x1e600
	s_add_i32 s61, 0, 0x10400
	s_waitcnt lgkmcnt(0)
	s_barrier
	s_load_dwordx4 s[44:47], s[14:15], 0xe8
	v_add_u32_e32 v203, 0, v49
	v_lshl_add_u64 v[110:111], v[20:21], 0, v[18:19]
	v_add3_u32 v205, s16, v51, v46
	s_load_dwordx2 s[64:65], s[14:15], 0xa0
	s_load_dwordx2 s[66:67], s[14:15], 0xb0
	v_add_u32_e32 v206, s61, v49
	v_or_b32_e32 v21, 64, v115
	v_or_b32_e32 v49, 0x80, v115
	v_or_b32_e32 v51, 0xc0, v115
	v_cmp_gt_u32_e64 s[24:25], v47, v113
	v_or_b32_e32 v47, 32, v46
	s_movk_i32 s26, 0x70
	v_bitop3_b32 v184, v46, v115, 16 bitop3:0x6c
	v_bitop3_b32 v183, v46, v21, 16 bitop3:0x6c
	v_bitop3_b32 v182, v46, v49, 16 bitop3:0x6c
	v_bitop3_b32 v181, v46, v51, 16 bitop3:0x6c
	v_bitop3_b32 v179, v47, v115, 48 bitop3:0x6c
	v_bitop3_b32 v178, v47, v21, 48 bitop3:0x6c
	v_bitop3_b32 v177, v47, v49, 48 bitop3:0x6c
	v_bitop3_b32 v176, v47, v51, 48 bitop3:0x6c
	v_or_b32_e32 v47, 64, v46
	s_movk_i32 s27, 0x50
	v_or_b32_e32 v46, 0x60, v46
	v_or_b32_e32 v53, v106, v113
	v_bitop3_b32 v208, v52, v21, s26 bitop3:0x6c
	v_bitop3_b32 v173, v47, v21, s27 bitop3:0x6c
	v_bitop3_b32 v166, v46, v21, s26 bitop3:0x6c
	v_mov_b32_e32 v21, s81
	v_mul_u32_u24_e32 v204, 0x110, v53
	v_mul_u32_u24_e32 v18, 0x48, v53
	v_add_u32_e32 v20, s16, v115
	s_movk_i32 s14, 0x80
	v_mad_u32_u24 v192, v113, s62, 0
	v_mad_u32_u24 v185, v113, s62, v21
	v_mul_u32_u24_e32 v193, 0x440, v70
	v_mul_u32_u24_e32 v194, 0x110, v50
	v_add_u32_e32 v197, 0x220, v195
	v_add_u32_e32 v198, 0x330, v195
	v_add_u32_e32 v199, 0x440, v195
	v_add_u32_e32 v200, 0x550, v195
	v_add_u32_e32 v201, 0x660, v195
	v_add_u32_e32 v202, 0x770, v195
	s_mov_b32 s57, 4
	v_mul_u32_u24_e32 v188, 0x90, v53
	v_lshl_add_u32 v189, v70, 3, 0
	v_add_u32_e32 v187, 0xfffffc00, v107
	v_bitop3_b32 v207, v52, v115, s26 bitop3:0x6c
	v_bitop3_b32 v209, v52, v49, s26 bitop3:0x6c
	v_bitop3_b32 v210, v52, v51, s26 bitop3:0x6c
	v_cmp_lt_i32_e64 s[16:17], -1, v48
	v_cmp_gt_u32_e64 s[38:39], s14, v112
	v_cmp_gt_u32_e64 s[18:19], v254, v113
	v_cmp_lt_u32_e64 s[20:21], v254, v113
	v_cmp_gt_u32_e64 s[22:23], v50, v113
	v_cmp_lt_i32_e64 s[36:37], 0, v48
	v_add_u32_e32 v191, 0x1100, v192
	v_cmp_eq_u32_e64 s[34:35], 1, v48
	v_cmp_lt_i32_e64 s[14:15], 1, v48
	v_add_u32_e32 v190, 0x2200, v192
	v_bitop3_b32 v174, v47, v115, s27 bitop3:0x6c
	v_bitop3_b32 v172, v47, v49, s27 bitop3:0x6c
	v_bitop3_b32 v171, v47, v51, s27 bitop3:0x6c
	v_cmp_eq_u32_e64 s[30:31], 2, v48
	v_cmp_lt_i32_e64 s[28:29], 2, v48
	v_bitop3_b32 v169, v46, v115, s26 bitop3:0x6c
	v_bitop3_b32 v165, v46, v49, s26 bitop3:0x6c
	v_bitop3_b32 v164, v46, v51, s26 bitop3:0x6c
	v_cmp_eq_u32_e64 s[26:27], 3, v48
	v_add_u32_e32 v180, 0x1100, v185
	v_add_u32_e32 v175, 0x2200, v185
	v_add_u32_e32 v168, 0x3300, v185
	v_add_lshl_u32 v211, v18, v254, 1
	s_add_i32 s83, s2, 0x700
	s_movk_i32 s84, 0x84
	s_movk_i32 s85, 0x7ff
	s_mov_b32 s86, 0xda24260
	v_mov_b32_e32 v212, 0xfffff800
	v_mov_b32_e32 v213, 0x80
	v_mov_b32_e32 v214, 0x7149f2ca
	v_add_u32_e32 v162, v20, v204
	s_mov_b32 s87, 0
	s_mov_b32 s88, 0
	v_readfirstlane_b32 s32, v84
	v_readfirstlane_b32 s93, v85
	v_readfirstlane_b32 s94, v86
	v_readfirstlane_b32 s95, v87
	v_readfirstlane_b32 s96, v108
	v_readfirstlane_b32 s97, v109
	s_nop 1
	v_subrev_u32_e32 v84, s32, v84
	v_add_u32_e32 v84, 0x40000, v84
	v_subrev_u32_e32 v108, s96, v108
	v_add_u32_e32 v108, 0x20000, v108
	v_lshl_add_u32 v152, v152, 12, v84
	v_lshl_add_u32 v136, v136, 12, v84
	v_lshl_add_u32 v137, v137, 12, v84
	v_lshl_add_u32 v138, v138, 12, v84
	v_lshl_add_u32 v139, v139, 12, v84
	v_lshl_add_u32 v140, v140, 12, v84
	v_lshl_add_u32 v142, v142, 12, v84
	v_lshl_add_u32 v144, v144, 12, v84
	v_lshl_add_u32 v145, v145, 11, v108
	s_waitcnt lgkmcnt(0)
	s_lshr_b32 s70, s2, 1
	s_and_b32 s71, s70, 31
	s_lshl_b32 s71, s71, 7
	s_or_b32 s71, s71, s53
	s_lshr_b32 s72, s70, 5
	s_lshl_b32 s72, s72, 7
	v_lshrrev_b32_e32 v20, 3, v0
	v_and_b32_e32 v21, 7, v0
	v_lshlrev_b32_e32 v21, 4, v21
	v_mul_u32_u24_e32 v213, 0x84, v20
	v_add_u32_e32 v213, v213, v21
	v_add_u32_e32 v212, s71, v20
	v_and_b32_e32 v46, 0x7ff, v212
	v_lshrrev_b32_e32 v212, 11, v212
	v_lshlrev_b32_e32 v212, 7, v212
	v_and_b32_e32 v47, 0x7f, v46
	v_or_b32_e32 v212, v212, v47
	v_lshrrev_b32_e32 v46, 7, v46
	v_lshl_or_b32 v212, v46, 8, v212
	v_lshlrev_b32_e32 v212, 11, v212
	v_add_u32_e32 v212, v212, v21
	v_add_u32_e32 v212, s72, v212
	s_branch .LBB0_975

; DEV int ltid() { int t = threadIdx.x; asm volatile("" : "+v"(t)); return t; }
; DEV void fill_store(CParams& p, int wg, int slot, int bufsel) {
;   extern __shared__ __attribute__((aligned(16))) char shm[];
;   const unsigned* T = (const unsigned*)(shm + FILL_LDS_OFF + bufsel * FILL_TB); const int tid = ltid(), nl = tid >> 3, cc = tid & 7;
;   const FillDesc d = fill_decode(p, wg, slot);
;   u32x4 v; v.x = T[nl * 33 + 4 * cc]; v.y = T[nl * 33 + 4 * cc + 1]; v.z = T[nl * 33 + 4 * cc + 2]; v.w = T[nl * 33 + 4 * cc + 3];
;   *(u32x4*)(d.dst + (long)perm_row(d.perm, d.n0 + nl) * 2048 + d.kh + 16 * cc) = v;
; }
.LBB0_975:
	s_add_i32 s89, s79, s88
	s_add_i32 s90, s79, s87
	s_add_i32 s62, s89, 0x137f
	s_add_i32 s70, s90, 0x480
	s_and_b64 s[68:69], s[54:55], exec
	s_cselect_b32 s62, s70, s62
	v_add_u32_e32 v21, s82, v213
	ds_read2_b32 v[46:47], v21 offset1:1
	ds_read2_b32 v[48:49], v21 offset0:2 offset1:3
	s_sub_u32 s70, s62, 64
	s_lshl_b32 s72, s70, 11
	s_lshl_b32 s70, s70, 12
	s_add_u32 s70, s32, s70
	s_addc_u32 s71, s93, 0
	s_add_u32 s72, s94, s72
	s_addc_u32 s73, s95, 0
	v_lshrrev_b32_e32 v20, 1, v152
	global_load_dword v251, v20, s[72:73] offset:1024
	global_load_dwordx2 v[126:127], v152, s[70:71] offset:2048
	v_lshrrev_b32_e32 v21, 1, v136
	global_load_dword v250, v21, s[72:73] offset:1024
	global_load_dwordx2 v[124:125], v136, s[70:71] offset:2048
	v_lshrrev_b32_e32 v20, 1, v137
	global_load_dword v249, v20, s[72:73] offset:1024
	global_load_dwordx2 v[122:123], v137, s[70:71] offset:2048
	v_lshrrev_b32_e32 v21, 1, v138
	global_load_dword v248, v21, s[72:73] offset:1024
	global_load_dwordx2 v[120:121], v138, s[70:71] offset:2048
	v_lshrrev_b32_e32 v20, 1, v139
	global_load_dword v247, v20, s[72:73] offset:1024
	global_load_dwordx2 v[118:119], v139, s[70:71] offset:2048
	v_lshrrev_b32_e32 v21, 1, v140
	global_load_dword v246, v21, s[72:73] offset:1024
	global_load_dwordx2 v[116:117], v140, s[70:71] offset:2048
	v_lshrrev_b32_e32 v20, 1, v142
	global_load_dword v241, v20, s[72:73] offset:1024
	global_load_dwordx2 v[114:115], v142, s[70:71] offset:2048
	v_lshrrev_b32_e32 v21, 1, v144
	global_load_dword v239, v21, s[72:73] offset:1024
	global_load_dwordx2 v[112:113], v144, s[70:71] offset:2048
	s_sub_u32 s70, s62, 64
	s_lshl_b32 s70, s70, 11
	s_add_u32 s70, s96, s70
	s_addc_u32 s71, s97, 0
	global_load_dwordx2 v[128:129], v145, s[70:71] offset:1024
	s_add_i32 s92, s83, 0xfffffc00
	s_lshr_b32 s70, s92, 8
	s_lshr_b32 s71, s70, 2
	s_lshl_b32 s71, s71, 23
	s_and_b32 s70, s70, 3
	s_lshl_b32 s70, s70, 9
	s_or_b32 s70, s70, s71
	s_add_u32 s72, s44, s70
	s_addc_u32 s73, s45, 0
	s_waitcnt lgkmcnt(0)
	global_store_dwordx4 v212, v[46:49], s[72:73]
	v_add_u32_e32 v216, v203, v207
	v_add_u32_e32 v220, v203, v209
	v_add_u32_e32 v217, v203, v208
	ds_read_b128 v[58:61], v216
	ds_read_b128 v[50:53], v217
	v_add_u32_e32 v221, v203, v210
	ds_read_b128 v[54:57], v220
	ds_read_b128 v[46:49], v221
	v_mov_b32_e32 v62, 0
	v_mov_b32_e32 v66, 0
	v_mov_b32_e32 v67, 0
	v_mov_b32_e32 v68, 0
	v_mov_b32_e32 v69, 0
	s_and_saveexec_b64 s[68:69], s[16:17]
	s_cbranch_execz .LBB0_986
	v_add_u32_e32 v18, v192, v184
	ds_read_b128 v[64:67], v18 offset:17408
	v_add_u32_e32 v18, v192, v183
	ds_read_b128 v[68:71], v18 offset:17408
	v_add_u32_e32 v18, v192, v182
	ds_read_b128 v[72:75], v18 offset:17408
	v_add_u32_e32 v18, v192, v181
	s_waitcnt lgkmcnt(2)
	v_mfma_f32_16x16x32_bf16 v[64:67], v[64:67], v[58:61], 0
	s_waitcnt lgkmcnt(1)
	v_mfma_f32_16x16x32_bf16 v[64:67], v[68:71], v[50:53], v[64:67]
	ds_read_b128 v[68:71], v18 offset:17408
	s_waitcnt lgkmcnt(1)
	v_mfma_f32_16x16x32_bf16 v[64:67], v[72:75], v[54:57], v[64:67]
	s_waitcnt lgkmcnt(0)
	v_mfma_f32_16x16x32_bf16 v[66:69], v[68:71], v[46:49], v[64:67]
	s_and_saveexec_b64 s[70:71], s[38:39]
	s_nop 6
	v_cndmask_b32_e64 v66, v66, 0, s[18:19]
	v_cndmask_b32_e64 v67, 0, v67, s[20:21]
	v_cndmask_b32_e64 v68, v68, 0, s[22:23]
	v_cndmask_b32_e64 v69, v69, 0, s[24:25]
	s_or_b64 exec, exec, s[70:71]

; DEV int ltid() { int t = threadIdx.x; asm volatile("" : "+v"(t)); return t; }
; DEV unsigned cvt_pk4_fp8(f32x4 v) { unsigned r = 0; r = __builtin_amdgcn_cvt_pk_fp8_f32(v[0], v[1], r, false); r = __builtin_amdgcn_cvt_pk_fp8_f32(v[2], v[3], r, true); return r; }
; DEV void fill_load(CParams& p, int wg, int slot, f32x4 (&ld)[4]) {
;   const FillDesc d = fill_decode(p, wg, slot); const int tid = ltid(), tx = tid & 15, ty = tid >> 4;
;   const float* sp = d.src + (long)(d.kh + 4 * ty) * d.ldsrc + d.n0 + 4 * tx;
; #pragma unroll
;   for (int r = 0; r < 4; ++r) ld[r] = *(const f32x4*)(sp + (long)r * d.ldsrc);
; }
; DEV void fill_write(const f32x4 (&ld)[4], int bufsel) {
;   extern __shared__ __attribute__((aligned(16))) char shm[];
;   unsigned* T = (unsigned*)(shm + FILL_LDS_OFF + bufsel * FILL_TB); const int tid = ltid(), tx = tid & 15, ty = tid >> 4;
;   constexpr float WS = (float)(1 << FP8_WSCALE_LOG2_);
; #pragma unroll
;   for (int j = 0; j < 4; ++j) T[(4 * tx + j) * 33 + ty] = cvt_pk4_fp8((f32x4){ld[0][j] * WS, ld[1][j] * WS, ld[2][j] * WS, ld[3][j] * WS});
; }
; DEV void fill_store(CParams& p, int wg, int slot, int bufsel) {
;   extern __shared__ __attribute__((aligned(16))) char shm[];
;   const unsigned* T = (const unsigned*)(shm + FILL_LDS_OFF + bufsel * FILL_TB); const int tid = ltid(), nl = tid >> 3, cc = tid & 7;
;   const FillDesc d = fill_decode(p, wg, slot);
;   u32x4 v; v.x = T[nl * 33 + 4 * cc]; v.y = T[nl * 33 + 4 * cc + 1]; v.z = T[nl * 33 + 4 * cc + 2]; v.w = T[nl * 33 + 4 * cc + 3];
;   *(u32x4*)(d.dst + (long)perm_row(d.perm, d.n0 + nl) * 2048 + d.kh + 16 * cc) = v;
; }
.LBB0_1007:
	v_mov_b32_e32 v4, v0
	s_lshl_b32 s62, s72, s62
	s_lshl_b32 s73, s72, 7
	v_ashrrev_i32_e32 v2, 2, v4
	s_and_b32 s62, s62, 0x780
	v_and_b32_e32 v2, -4, v2
	s_and_b32 s71, s71, s73
	v_add_u32_e32 v2, s62, v2
	s_or_b32 s71, s71, s53
	v_mad_i64_i32 v[2:3], s[72:73], s70, v2, 0
	v_lshl_add_u64 v[2:3], v[2:3], 2, s[68:69]
	s_lshl_b32 s62, s71, 2
	v_lshlrev_b32_e32 v4, 4, v4
	v_lshl_add_u64 v[2:3], v[2:3], 0, s[62:63]
	v_and_b32_e32 v18, 0xf0, v4
	v_lshl_add_u64 v[2:3], v[2:3], 0, v[18:19]
	s_lshl_b32 s62, s70, 2
	v_lshl_add_u64 v[4:5], v[2:3], 0, s[62:63]
	global_load_dwordx4 v[10:13], v[2:3], off
	global_load_dwordx4 v[14:17], v[4:5], off
	v_lshl_add_u64 v[2:3], v[4:5], 0, s[62:63]
	v_lshl_add_u64 v[6:7], v[2:3], 0, s[62:63]
	s_add_i32 s62, s89, 0x133f
	s_add_i32 s70, s90, 0x4c0
	s_and_b64 s[68:69], s[54:55], exec
	s_cselect_b32 s62, s70, s62
	s_sub_u32 s70, s62, 64
	s_lshl_b32 s72, s70, 11
	s_lshl_b32 s70, s70, 12
	s_add_u32 s70, s32, s70
	s_addc_u32 s71, s93, 0
	s_add_u32 s72, s94, s72
	s_addc_u32 s73, s95, 0
	global_load_dwordx4 v[2:5], v[2:3], off
	s_nop 0
	global_load_dwordx4 v[6:9], v[6:7], off
	s_waitcnt lgkmcnt(0)
	s_barrier
	v_add_u32_e32 v21, s78, v213
	ds_read2_b32 v[46:47], v21 offset1:1
	ds_read2_b32 v[48:49], v21 offset0:2 offset1:3
	v_lshrrev_b32_e32 v20, 1, v152
	global_load_dword v170, v20, s[72:73] offset:1024
	global_load_dwordx2 v[102:103], v152, s[70:71] offset:2048
	v_lshrrev_b32_e32 v21, 1, v136
	global_load_dword v167, v21, s[72:73] offset:1024
	global_load_dwordx2 v[100:101], v136, s[70:71] offset:2048
	v_lshrrev_b32_e32 v20, 1, v137
	global_load_dword v163, v20, s[72:73] offset:1024
	global_load_dwordx2 v[98:99], v137, s[70:71] offset:2048
	v_lshrrev_b32_e32 v21, 1, v138
	global_load_dword v161, v21, s[72:73] offset:1024
	global_load_dwordx2 v[96:97], v138, s[70:71] offset:2048
	v_lshrrev_b32_e32 v20, 1, v139
	global_load_dword v160, v20, s[72:73] offset:1024
	global_load_dwordx2 v[94:95], v139, s[70:71] offset:2048
	v_lshrrev_b32_e32 v21, 1, v140
	global_load_dword v159, v21, s[72:73] offset:1024
	global_load_dwordx2 v[92:93], v140, s[70:71] offset:2048
	v_lshrrev_b32_e32 v20, 1, v142
	global_load_dword v158, v20, s[72:73] offset:1024
	global_load_dwordx2 v[90:91], v142, s[70:71] offset:2048
	v_lshrrev_b32_e32 v21, 1, v144
	global_load_dword v157, v21, s[72:73] offset:1024
	global_load_dwordx2 v[88:89], v144, s[70:71] offset:2048
	s_sub_u32 s70, s62, 64
	s_lshl_b32 s70, s70, 11
	s_add_u32 s70, s96, s70
	s_addc_u32 s71, s97, 0
	global_load_dwordx2 v[104:105], v145, s[70:71] offset:1024
	s_add_i32 s92, s83, 0xfffffd00
	s_lshr_b32 s70, s92, 8
	s_lshr_b32 s71, s70, 2
	s_lshl_b32 s71, s71, 23
	s_and_b32 s70, s70, 3
	s_lshl_b32 s70, s70, 9
	s_or_b32 s70, s70, s71
	s_add_u32 s72, s44, s70
	s_addc_u32 s73, s45, 0
	s_waitcnt lgkmcnt(0)
	global_store_dwordx4 v212, v[46:49], s[72:73]
	v_add_u32_e32 v242, v206, v207
	v_add_u32_e32 v244, v206, v209
	v_add_u32_e32 v243, v206, v208
	ds_read_b128 v[58:61], v242
	ds_read_b128 v[54:57], v243
	v_add_u32_e32 v245, v206, v210
	ds_read_b128 v[50:53], v244
	ds_read_b128 v[46:49], v245
	v_mov_b32_e32 v62, 0
	v_mov_b32_e32 v66, 0
	v_mov_b32_e32 v67, 0
	v_mov_b32_e32 v68, 0
	v_mov_b32_e32 v69, 0
	s_and_saveexec_b64 s[68:69], s[16:17]
	s_cbranch_execz .LBB0_1018
	v_add_u32_e32 v18, v185, v184
	ds_read_b128 v[64:67], v18
	v_add_u32_e32 v18, v185, v183
	ds_read_b128 v[68:71], v18
	v_add_u32_e32 v18, v185, v182
	ds_read_b128 v[72:75], v18
	v_add_u32_e32 v18, v185, v181
	s_waitcnt lgkmcnt(2)
	v_mfma_f32_16x16x32_bf16 v[64:67], v[64:67], v[58:61], 0
	s_waitcnt lgkmcnt(1)
	v_mfma_f32_16x16x32_bf16 v[64:67], v[68:71], v[54:57], v[64:67]
	ds_read_b128 v[68:71], v18
	s_waitcnt lgkmcnt(1)
	v_mfma_f32_16x16x32_bf16 v[64:67], v[72:75], v[50:53], v[64:67]
	s_waitcnt lgkmcnt(0)
	v_mfma_f32_16x16x32_bf16 v[66:69], v[68:71], v[46:49], v[64:67]
	s_and_saveexec_b64 s[70:71], s[38:39]
	s_nop 6
	v_cndmask_b32_e64 v66, v66, 0, s[18:19]
	v_cndmask_b32_e64 v67, 0, v67, s[20:21]
	v_cndmask_b32_e64 v68, v68, 0, s[22:23]
	v_cndmask_b32_e64 v69, v69, 0, s[24:25]
	s_or_b64 exec, exec, s[70:71]

; DEV FillDesc fill_decode(CParams& p, int wg, int slot) {
;   const int h = slot * 256 + wg, t = h >> 1, half = h & 1; FillDesc d;
;   if (t < NE * 512) { const int e = t >> 9, r = t & 511; d.src = p.w_gu + (long)e * 2048 * 4096; d.ldsrc = 4096; d.dst = p.wt_gu8 + (long)e * 4096 * 2048; d.perm = 2; d.n0 = (r & 31) * 128 + 64 * half; d.kh = (r >> 5) * 128; }
;   else { const int v = t - NE * 512, e = v >> 8, r = v & 255; d.src = p.w_dn + (long)e * 2048 * 2048; d.ldsrc = 2048; d.dst = p.wt_dn8 + (long)e * 2048 * 2048; d.perm = 0; d.n0 = (r & 15) * 128 + 64 * half; d.kh = (r >> 4) * 128; }
;   return d;
; DEV void hgrn_unit(CParams& p, int u, int wg, bool fill) {
;     ...
;   HG_STEP(66, true, true, fldA);
;   HG_MMA(67, true);
;   __syncthreads();
;   if (fill && FILL_HG == 67) fill_store(p, wg, 66, 0);
.LBB0_1039:
	v_mov_b32_e32 v212, 0xfffff800
	v_mov_b32_e32 v213, 0x80
	s_add_i32 s68, s2, 0x4100
	s_ashr_i32 s57, s68, 1
	s_cmpk_lt_i32 s57, 0x4000
	v_mov_b32_e32 v18, v0
	s_cselect_b64 s[64:65], -1, 0
	s_cmpk_gt_i32 s57, 0x3fff
	s_cbranch_scc0 .LBB0_1041
	s_add_i32 s61, s57, 0xffffc000
	s_lshr_b32 s62, s61, 8
	s_mov_b32 s63, 0
	s_lshl_b64 s[62:63], s[62:63], 22
	s_add_u32 s62, s46, s62
	s_addc_u32 s63, s47, s63
	s_mov_b32 s61, 3
	s_movk_i32 s66, 0x780
	s_cbranch_execz .LBB0_1042
	s_branch .LBB0_1043
